# speedup vs baseline: 1.0096x; 1.0041x over previous
.LBB1_8:
	s_or_b64 exec, exec, s[4:5]
	s_waitcnt vmcnt(0) lgkmcnt(0)
	v_lshl_or_b32 v186, s19, 6, v1
	v_ashrrev_i32_e32 v187, 31, v186
	v_lshl_add_u64 v[186:187], v[186:187], 2, s[6:7]
	global_load_dword v175, v[186:187], off
	v_mov_b32_e32 v184, 1
	v_lshl_add_u32 v180, v176, 2, v172
	v_lshl_add_u32 v181, v177, 2, v172
	v_lshl_add_u32 v182, v178, 2, v172
	v_lshl_add_u32 v183, v179, 2, v172
	s_waitcnt lgkmcnt(0)
	ds_add_u32 v180, v184
	ds_add_u32 v181, v184
	ds_add_u32 v182, v184
	ds_add_u32 v183, v184
	s_waitcnt lgkmcnt(0)
	ds_read_b32 v151, v173
	s_waitcnt lgkmcnt(0)
	v_cvt_f32_i32_e32 v185, v151
	ds_write_b32 v173, v185 offset:256
	v_add_u32_e32 v10, v172, v2
	s_waitcnt vmcnt(1) lgkmcnt(0)
	s_barrier
	s_nop 0
	s_nop 0
	ds_read_b128 v[18:21], v10 offset:256
	ds_read_b128 v[22:25], v10 offset:288
	ds_read_b128 v[82:85], v10 offset:320
	ds_read_b128 v[86:89], v10 offset:352
	ds_read_b128 v[74:77], v10 offset:384
	ds_read_b128 v[78:81], v10 offset:416
	ds_read_b128 v[2:5], v213 offset:32768
	ds_read_b128 v[6:9], v213 offset:0
	ds_read_b128 v[66:69], v10 offset:448
	ds_read_b128 v[70:73], v10 offset:480
	ds_read_b128 v[10:13], v213 offset:1024
	s_waitcnt lgkmcnt(3)
	v_pk_mul_f32 v[26:27], v[8:9], v[20:21]
	v_pk_mul_f32 v[28:29], v[6:7], v[18:19]
	ds_read_b128 v[14:17], v213 offset:8192
	s_waitcnt lgkmcnt(1)
	v_pk_mul_f32 v[12:13], v[12:13], v[24:25]
	v_pk_mul_f32 v[10:11], v[10:11], v[22:23]
	v_pk_fma_f32 v[30:31], v[8:9], v[20:21], v[12:13]
	v_pk_fma_f32 v[32:33], v[6:7], v[18:19], v[10:11]
	v_cvt_pk_bf16_f32 v9, v12, v13
	v_cvt_pk_bf16_f32 v7, v26, v27
	v_cvt_pk_bf16_f32 v8, v10, v11
	v_cvt_pk_bf16_f32 v6, v28, v29
	ds_read_b128 v[10:13], v213 offset:33792
	s_nop 0
	v_mfma_f32_32x32x16_bf16 v[34:49], v[2:5], v[6:9], 0
	ds_read_b128 v[6:9], v213 offset:9216
	s_waitcnt lgkmcnt(2)
	v_mul_f32_e32 v26, v16, v20
	v_mul_f32_e32 v27, v17, v21
	v_pk_mul_f32 v[50:51], v[14:15], v[18:19]
	s_mov_b32 s4, 0x3727c5ac
	s_waitcnt lgkmcnt(0)
	v_pk_mul_f32 v[8:9], v[8:9], v[24:25]
	v_pk_mul_f32 v[28:29], v[6:7], v[22:23]
	v_pk_fma_f32 v[90:91], v[16:17], v[20:21], v[8:9]
	v_pk_fma_f32 v[92:93], v[14:15], v[18:19], v[28:29]
	ds_read_b128 v[14:17], v213 offset:2048
	v_cvt_pk_bf16_f32 v9, v8, v9
	v_cvt_pk_bf16_f32 v7, v26, v27
	v_cvt_pk_bf16_f32 v8, v28, v29
	ds_read_b128 v[26:29], v213 offset:3072
	v_cvt_pk_bf16_f32 v6, v50, v51
	s_waitcnt lgkmcnt(1)
	v_pk_mul_f32 v[94:95], v[14:15], v[82:83]
	s_mov_b32 s0, 0x3c800000
	v_mfma_f32_32x32x16_bf16 v[50:65], v[2:5], v[6:9], 0
	v_mul_f32_e32 v2, v16, v84
	v_mul_f32_e32 v3, v17, v85
	s_waitcnt lgkmcnt(0)
	v_mul_f32_e32 v4, v28, v88
	v_mul_f32_e32 v5, v29, v89
	v_pk_mul_f32 v[6:7], v[26:27], v[86:87]
	v_pk_fma_f32 v[8:9], v[16:17], v[84:85], v[4:5]
	v_cvt_pk_bf16_f32 v3, v2, v3
	v_pk_fma_f32 v[14:15], v[14:15], v[82:83], v[6:7]
	v_pk_add_f32 v[26:27], v[8:9], v[30:31]
	v_cvt_pk_bf16_f32 v5, v4, v5
	v_cvt_pk_bf16_f32 v4, v6, v7
	ds_read_b128 v[6:9], v213 offset:10240
	v_pk_add_f32 v[28:29], v[14:15], v[32:33]
	ds_read_b128 v[14:17], v213 offset:11264
	v_cvt_pk_bf16_f32 v2, v94, v95
	s_waitcnt lgkmcnt(1)
	v_pk_mul_f32 v[30:31], v[6:7], v[82:83]
	v_mov_b64_e32 v[152:153], s[4:5]
	v_mfma_f32_32x32x16_bf16 v[34:49], v[10:13], v[2:5], v[34:49]
	v_mul_f32_e32 v2, v8, v84
	v_mul_f32_e32 v3, v9, v85
	s_waitcnt lgkmcnt(0)
	v_mul_f32_e32 v4, v16, v88
	v_mul_f32_e32 v5, v17, v89
	v_pk_mul_f32 v[14:15], v[14:15], v[86:87]
	v_pk_fma_f32 v[8:9], v[8:9], v[84:85], v[4:5]
	v_pk_fma_f32 v[6:7], v[6:7], v[82:83], v[14:15]
	v_cvt_pk_bf16_f32 v5, v4, v5
	v_cvt_pk_bf16_f32 v3, v2, v3
	v_cvt_pk_bf16_f32 v4, v14, v15
	v_pk_add_f32 v[32:33], v[8:9], v[90:91]
	v_pk_add_f32 v[90:91], v[6:7], v[92:93]
	ds_read_b128 v[6:9], v213 offset:34816
	ds_read_b128 v[14:17], v213 offset:4096
	v_cvt_pk_bf16_f32 v2, v30, v31
	s_mov_b32 s13, 0
	s_mov_b64 s[6:7], 0
	v_mfma_f32_32x32x16_bf16 v[50:65], v[10:13], v[2:5], v[50:65]
	ds_read_b128 v[2:5], v213 offset:5120
	ds_read_b128 v[10:13], v213 offset:12288
	s_waitcnt lgkmcnt(2)
	v_pk_mul_f32 v[30:31], v[16:17], v[76:77]
	v_pk_mul_f32 v[92:93], v[14:15], v[74:75]
	s_waitcnt lgkmcnt(1)
	v_pk_mul_f32 v[4:5], v[4:5], v[80:81]
	v_pk_mul_f32 v[94:95], v[2:3], v[78:79]
	v_pk_fma_f32 v[2:3], v[16:17], v[76:77], v[4:5]
	v_cvt_pk_bf16_f32 v5, v4, v5
	v_pk_add_f32 v[96:97], v[2:3], v[26:27]
	v_cvt_pk_bf16_f32 v3, v30, v31
	v_cvt_pk_bf16_f32 v4, v94, v95
	v_cvt_pk_bf16_f32 v2, v92, v93
	v_pk_fma_f32 v[14:15], v[14:15], v[74:75], v[94:95]
	s_waitcnt lgkmcnt(0)
	v_pk_mul_f32 v[30:31], v[10:11], v[74:75]
	v_mfma_f32_32x32x16_bf16 v[34:49], v[6:9], v[2:5], v[34:49]
	ds_read_b128 v[2:5], v213 offset:13312
	v_add_f32_e32 v98, v14, v28
	v_add_f32_e32 v99, v15, v29
	ds_read_b128 v[14:17], v213 offset:35840
	v_pk_mul_f32 v[26:27], v[12:13], v[76:77]
	s_waitcnt lgkmcnt(1)
	v_pk_mul_f32 v[4:5], v[4:5], v[80:81]
	v_pk_mul_f32 v[28:29], v[2:3], v[78:79]
	v_pk_fma_f32 v[2:3], v[12:13], v[76:77], v[4:5]
	v_pk_fma_f32 v[10:11], v[10:11], v[74:75], v[28:29]
	v_pk_add_f32 v[32:33], v[2:3], v[32:33]
	v_pk_add_f32 v[92:93], v[10:11], v[90:91]
	ds_read_b128 v[10:13], v213 offset:6144
	v_cvt_pk_bf16_f32 v5, v4, v5
	v_cvt_pk_bf16_f32 v3, v26, v27
	v_cvt_pk_bf16_f32 v4, v28, v29
	ds_read_b128 v[26:29], v213 offset:7168
	v_cvt_pk_bf16_f32 v2, v30, v31
	s_waitcnt lgkmcnt(1)
	v_pk_mul_f32 v[30:31], v[10:11], v[66:67]
	v_mfma_f32_32x32x16_bf16 v[50:65], v[6:9], v[2:5], v[50:65]
	v_mul_f32_e32 v2, v12, v68
	v_mul_f32_e32 v3, v13, v69
	s_waitcnt lgkmcnt(0)
	v_mul_f32_e32 v4, v28, v72
	v_mul_f32_e32 v5, v29, v73
	v_pk_mul_f32 v[6:7], v[26:27], v[70:71]
	v_pk_fma_f32 v[8:9], v[12:13], v[68:69], v[4:5]
	v_cvt_pk_bf16_f32 v3, v2, v3
	v_pk_fma_f32 v[10:11], v[10:11], v[66:67], v[6:7]
	v_pk_add_f32 v[94:95], v[8:9], v[96:97]
	v_cvt_pk_bf16_f32 v5, v4, v5
	v_cvt_pk_bf16_f32 v4, v6, v7
	ds_read_b128 v[6:9], v213 offset:14336
	v_pk_add_f32 v[96:97], v[10:11], v[98:99]
	ds_read_b128 v[10:13], v213 offset:15360
	v_cvt_pk_bf16_f32 v2, v30, v31
	s_waitcnt lgkmcnt(1)
	v_pk_mul_f32 v[30:31], v[6:7], v[66:67]
	v_mfma_f32_32x32x16_bf16 v[34:49], v[14:17], v[2:5], v[34:49]
	s_waitcnt lgkmcnt(0)
	v_mul_f32_e32 v10, v10, v70
	v_mul_f32_e32 v11, v11, v71
	v_mul_f32_e32 v2, v8, v68
	v_mul_f32_e32 v3, v9, v69
	v_pk_mul_f32 v[4:5], v[12:13], v[72:73]
	v_pk_fma_f32 v[6:7], v[6:7], v[66:67], v[10:11]
	v_pk_fma_f32 v[8:9], v[8:9], v[68:69], v[4:5]
	v_pk_add_f32 v[92:93], v[6:7], v[92:93]
	v_cvt_pk_bf16_f32 v3, v2, v3
	v_pk_add_f32 v[90:91], v[8:9], v[32:33]
	v_cvt_pk_bf16_f32 v5, v4, v5
	v_cvt_pk_bf16_f32 v4, v10, v11
	ds_read_b128 v[26:29], v213 offset:36864
	ds_read_b128 v[6:9], v213 offset:16384
	v_cvt_pk_bf16_f32 v2, v30, v31
	ds_read_b128 v[98:101], v213 offset:25600
	ds_read_b128 v[102:105], v213 offset:37888
	v_mfma_f32_32x32x16_bf16 v[50:65], v[14:17], v[2:5], v[50:65]
	ds_read_b128 v[2:5], v213 offset:17408
	ds_read_b128 v[30:33], v213 offset:24576
	s_waitcnt lgkmcnt(4)
	v_pk_mul_f32 v[12:13], v[6:7], v[18:19]
	v_pk_mul_f32 v[10:11], v[8:9], v[20:21]
	s_waitcnt lgkmcnt(1)
	v_pk_mul_f32 v[14:15], v[2:3], v[22:23]
	v_pk_mul_f32 v[22:23], v[98:99], v[22:23]
	v_pk_fma_f32 v[112:113], v[6:7], v[18:19], v[14:15]
	s_waitcnt lgkmcnt(0)
	v_pk_mul_f32 v[114:115], v[30:31], v[18:19]
	v_pk_fma_f32 v[118:119], v[30:31], v[18:19], v[22:23]
	v_pk_mul_f32 v[4:5], v[4:5], v[24:25]
	v_pk_mul_f32 v[106:107], v[32:33], v[20:21]
	v_pk_mul_f32 v[24:25], v[100:101], v[24:25]
	ds_read_b128 v[98:101], v213 offset:18432
	v_cvt_pk_bf16_f32 v19, v106, v107
	ds_read_b128 v[106:109], v213 offset:19456
	v_pk_fma_f32 v[110:111], v[8:9], v[20:21], v[4:5]
	v_cvt_pk_bf16_f32 v5, v4, v5
	v_cvt_pk_bf16_f32 v3, v10, v11
	v_cvt_pk_bf16_f32 v4, v14, v15
	s_waitcnt lgkmcnt(0)
	v_pk_mul_f32 v[106:107], v[106:107], v[86:87]
	v_cvt_pk_bf16_f32 v2, v12, v13
	v_pk_mul_f32 v[120:121], v[98:99], v[82:83]
	v_pk_mul_f32 v[108:109], v[108:109], v[88:89]
	v_pk_fma_f32 v[98:99], v[98:99], v[82:83], v[106:107]
	v_mfma_f32_32x32x16_bf16 v[2:17], v[26:29], v[2:5], 0
	v_cvt_pk_bf16_f32 v18, v114, v115
	v_mul_f32_e32 v114, v100, v84
	v_mul_f32_e32 v115, v101, v85
	v_fma_f32 v100, v100, v84, v108
	v_fma_f32 v101, v101, v85, v109
	v_pk_add_f32 v[124:125], v[98:99], v[112:113]
	v_pk_add_f32 v[122:123], v[100:101], v[110:111]
	v_cvt_pk_bf16_f32 v101, v108, v109
	v_cvt_pk_bf16_f32 v100, v106, v107
	ds_read_b128 v[106:109], v213 offset:26624
	v_pk_fma_f32 v[116:117], v[32:33], v[20:21], v[24:25]
	v_cvt_pk_bf16_f32 v21, v24, v25
	v_cvt_pk_bf16_f32 v20, v22, v23
	ds_read_b128 v[110:113], v213 offset:27648
	v_cvt_pk_bf16_f32 v99, v114, v115
	v_mfma_f32_32x32x16_bf16 v[18:33], v[26:29], v[18:21], 0
	v_cvt_pk_bf16_f32 v98, v120, v121
	s_waitcnt lgkmcnt(1)
	v_mul_f32_e32 v114, v106, v82
	v_mul_f32_e32 v115, v107, v83
	s_waitcnt lgkmcnt(0)
	v_pk_mul_f32 v[86:87], v[110:111], v[86:87]
	v_pk_mul_f32 v[88:89], v[112:113], v[88:89]
	v_pk_fma_f32 v[82:83], v[106:107], v[82:83], v[86:87]
	v_mfma_f32_32x32x16_bf16 v[2:17], v[102:105], v[98:101], v[2:17]
	v_mul_f32_e32 v98, v108, v84
	v_mul_f32_e32 v99, v109, v85
	v_fma_f32 v84, v108, v84, v88
	v_fma_f32 v85, v109, v85, v89
	v_add_f32_e32 v108, v82, v118
	v_add_f32_e32 v109, v83, v119
	v_cvt_pk_bf16_f32 v83, v98, v99
	v_pk_add_f32 v[106:107], v[84:85], v[116:117]
	v_cvt_pk_bf16_f32 v85, v88, v89
	v_cvt_pk_bf16_f32 v84, v86, v87
	ds_read_b128 v[86:89], v213 offset:38912
	ds_read_b128 v[98:101], v213 offset:20480
	v_cvt_pk_bf16_f32 v82, v114, v115
	s_waitcnt lgkmcnt(0)
	v_pk_mul_f32 v[110:111], v[100:101], v[76:77]
	v_mfma_f32_32x32x16_bf16 v[18:33], v[102:105], v[82:85], v[18:33]
	ds_read_b128 v[82:85], v213 offset:21504
	ds_read_b128 v[102:105], v213 offset:28672
	v_mul_f32_e32 v112, v98, v74
	v_mul_f32_e32 v113, v99, v75
	s_waitcnt lgkmcnt(1)
	v_pk_mul_f32 v[84:85], v[84:85], v[80:81]
	v_pk_mul_f32 v[114:115], v[82:83], v[78:79]
	v_pk_fma_f32 v[82:83], v[100:101], v[76:77], v[84:85]
	v_cvt_pk_bf16_f32 v85, v84, v85
	v_pk_add_f32 v[116:117], v[82:83], v[122:123]
	v_cvt_pk_bf16_f32 v83, v110, v111
	v_cvt_pk_bf16_f32 v84, v114, v115
	v_cvt_pk_bf16_f32 v82, v112, v113
	v_pk_fma_f32 v[98:99], v[98:99], v[74:75], v[114:115]
	s_waitcnt lgkmcnt(0)
	v_pk_mul_f32 v[112:113], v[102:103], v[74:75]
	v_mfma_f32_32x32x16_bf16 v[2:17], v[86:89], v[82:85], v[2:17]
	ds_read_b128 v[82:85], v213 offset:29696
	v_add_f32_e32 v118, v98, v124
	v_add_f32_e32 v119, v99, v125
	v_mul_f32_e32 v110, v104, v76
	v_mul_f32_e32 v111, v105, v77
	ds_read_b128 v[98:101], v213 offset:39936
	s_waitcnt lgkmcnt(1)
	v_pk_mul_f32 v[78:79], v[82:83], v[78:79]
	v_pk_mul_f32 v[80:81], v[84:85], v[80:81]
	v_pk_fma_f32 v[74:75], v[102:103], v[74:75], v[78:79]
	v_pk_fma_f32 v[76:77], v[104:105], v[76:77], v[80:81]
	v_pk_add_f32 v[104:105], v[74:75], v[108:109]
	v_pk_add_f32 v[102:103], v[76:77], v[106:107]
	v_cvt_pk_bf16_f32 v77, v80, v81
	v_cvt_pk_bf16_f32 v76, v78, v79
	ds_read_b128 v[78:81], v213 offset:22528
	ds_read_b128 v[82:85], v213 offset:23552
	v_cvt_pk_bf16_f32 v75, v110, v111
	v_cvt_pk_bf16_f32 v74, v112, v113
	s_waitcnt lgkmcnt(0)
	v_pk_mul_f32 v[82:83], v[82:83], v[70:71]
	v_mfma_f32_32x32x16_bf16 v[18:33], v[86:89], v[74:77], v[18:33]
	v_mul_f32_e32 v74, v80, v68
	v_mul_f32_e32 v75, v81, v69
	v_mul_f32_e32 v76, v84, v72
	v_mul_f32_e32 v77, v85, v73
	v_mul_f32_e32 v86, v78, v66
	v_mul_f32_e32 v87, v79, v67
	v_pk_fma_f32 v[80:81], v[80:81], v[68:69], v[76:77]
	v_pk_fma_f32 v[78:79], v[78:79], v[66:67], v[82:83]
	v_cvt_pk_bf16_f32 v75, v74, v75
	v_pk_add_f32 v[88:89], v[80:81], v[116:117]
	v_pk_add_f32 v[106:107], v[78:79], v[118:119]
	ds_read_b128 v[78:81], v213 offset:30720
	v_cvt_pk_bf16_f32 v77, v76, v77
	v_cvt_pk_bf16_f32 v76, v82, v83
	ds_read_b128 v[82:85], v213 offset:31744
	v_cvt_pk_bf16_f32 v74, v86, v87
	s_waitcnt lgkmcnt(0)
	v_pk_mul_f32 v[72:73], v[84:85], v[72:73]
	v_mfma_f32_32x32x16_bf16 v[2:17], v[98:101], v[74:77], v[2:17]
	v_mul_f32_e32 v74, v80, v68
	v_mul_f32_e32 v75, v81, v69
	v_fma_f32 v68, v80, v68, v72
	v_fma_f32 v69, v81, v69, v73
	v_mul_f32_e32 v70, v82, v70
	v_mul_f32_e32 v71, v83, v71
	v_pk_add_f32 v[84:85], v[68:69], v[102:103]
	v_cvt_pk_bf16_f32 v69, v72, v73
	v_pk_mov_b32 v[72:73], v[96:97], v[94:95] op_sel:[1,0]
	v_mov_b32_e32 v97, v95
	v_pk_add_f32 v[72:73], v[72:73], v[96:97]
	v_pk_mul_f32 v[76:77], v[78:79], v[66:67]
	v_pk_fma_f32 v[66:67], v[78:79], v[66:67], v[70:71]
	v_pk_add_f32 v[72:73], v[72:73], v[72:73] op_sel:[0,1] op_sel_hi:[1,0]
	v_pk_add_f32 v[86:87], v[66:67], v[104:105]
	v_mov_b32_e32 v66, v72
	s_nop 1
	v_permlane32_swap_b32_e32 v72, v66
	v_add_f32_e32 v66, v72, v66
	v_cvt_pk_bf16_f32 v67, v74, v75
	v_rcp_f32_e32 v74, v66
	v_cvt_pk_bf16_f32 v68, v70, v71
	v_cvt_pk_bf16_f32 v66, v76, v77
	v_pk_mul_f32 v[70:71], v[46:47], v[74:75] op_sel_hi:[1,0]
	s_nop 0
	v_mfma_f32_32x32x16_bf16 v[18:33], v[98:101], v[66:69], v[18:33]
	v_mul_f32_e32 v66, v42, v74
	v_mul_f32_e32 v67, v43, v74
	v_pk_mov_b32 v[42:43], v[92:93], v[90:91] op_sel:[1,0]
	v_mov_b32_e32 v93, v91
	v_pk_add_f32 v[42:43], v[42:43], v[92:93]
	v_pk_mul_f32 v[68:69], v[44:45], v[74:75] op_sel_hi:[1,0]
	v_pk_add_f32 v[42:43], v[42:43], v[42:43] op_sel:[0,1] op_sel_hi:[1,0]
	v_pk_mov_b32 v[44:45], v[106:107], v[88:89] op_sel:[1,0]
	v_mov_b32_e32 v43, v42
	s_nop 1
	v_permlane32_swap_b32_e32 v42, v43
	v_add_f32_e32 v42, v42, v43
	v_rcp_f32_e32 v42, v42
	v_mov_b32_e32 v107, v89
	v_pk_add_f32 v[44:45], v[44:45], v[106:107]
	v_pk_mul_f32 v[72:73], v[48:49], v[74:75] op_sel_hi:[1,0]
	v_pk_add_f32 v[44:45], v[44:45], v[44:45] op_sel:[0,1] op_sel_hi:[1,0]
	v_pk_mul_f32 v[36:37], v[36:37], v[74:75] op_sel_hi:[1,0]
	v_pk_mul_f32 v[38:39], v[38:39], v[74:75] op_sel_hi:[1,0]
	v_pk_mul_f32 v[40:41], v[40:41], v[74:75] op_sel_hi:[1,0]
	v_pk_mul_f32 v[34:35], v[34:35], v[74:75] op_sel_hi:[1,0]
	v_pk_mul_f32 v[74:75], v[58:59], v[42:43] op_sel_hi:[1,0]
	v_pk_mul_f32 v[78:79], v[60:61], v[42:43] op_sel_hi:[1,0]
	v_pk_mul_f32 v[80:81], v[62:63], v[42:43] op_sel_hi:[1,0]
	v_pk_mul_f32 v[82:83], v[64:65], v[42:43] op_sel_hi:[1,0]
	v_pk_mul_f32 v[92:93], v[52:53], v[42:43] op_sel_hi:[1,0]
	v_mov_b32_e32 v43, v44
	s_nop 1
	v_permlane32_swap_b32_e32 v44, v43
	v_add_f32_e32 v43, v44, v43
	v_rcp_f32_e32 v76, v43
	v_pk_mul_f32 v[96:97], v[54:55], v[42:43] op_sel_hi:[1,0]
	v_pk_mul_f32 v[94:95], v[56:57], v[42:43] op_sel_hi:[1,0]
	v_pk_mul_f32 v[98:99], v[50:51], v[42:43] op_sel_hi:[1,0]
	v_pk_mul_f32 v[100:101], v[4:5], v[76:77] op_sel_hi:[1,0]
	v_pk_mov_b32 v[4:5], v[86:87], v[84:85] op_sel:[1,0]
	v_mov_b32_e32 v87, v85
	v_pk_add_f32 v[4:5], v[4:5], v[86:87]
	v_pk_mul_f32 v[102:103], v[6:7], v[76:77] op_sel_hi:[1,0]
	v_pk_add_f32 v[104:105], v[4:5], v[4:5] op_sel:[0,1] op_sel_hi:[1,0]
	v_cvt_pk_bf16_f32 v7, v40, v41
	ds_read_b128 v[84:87], v150 offset:52224
	ds_read_b128 v[50:53], v150 offset:35840
	ds_read_b128 v[54:57], v150 offset:36864
	ds_read_b128 v[58:61], v150 offset:37888
	ds_read_b128 v[62:65], v150 offset:38912
	v_cvt_pk_bf16_f32 v6, v38, v39
	v_cvt_pk_bf16_f32 v5, v36, v37
	v_cvt_pk_bf16_f32 v4, v34, v35
	ds_read_b128 v[88:91], v150 offset:53248
	ds_read_b128 v[34:37], v150 offset:39936
	ds_read_b128 v[38:41], v150 offset:40960
	ds_read_b128 v[42:45], v150 offset:41984
	ds_read_b128 v[46:49], v150 offset:43008
	v_cvt_pk_bf16_f32 v95, v94, v95
	v_cvt_pk_bf16_f32 v94, v96, v97
	v_cvt_pk_bf16_f32 v93, v92, v93
	v_cvt_pk_bf16_f32 v92, v98, v99
	s_waitcnt lgkmcnt(5)
	v_mfma_f32_32x32x16_bf16 v[50:65], v[84:87], v[4:7], v[50:65]
	v_mul_f32_e32 v10, v10, v76
	v_mul_f32_e32 v11, v11, v76
	v_mul_f32_e32 v12, v12, v76
	v_mul_f32_e32 v13, v13, v76
	v_mul_f32_e32 v8, v8, v76
	v_mul_f32_e32 v9, v9, v76
	v_mov_b32_e32 v77, v104
	s_nop 1
	v_permlane32_swap_b32_e32 v104, v77
	v_cvt_pk_bf16_f32 v73, v72, v73
	s_waitcnt lgkmcnt(0)
	v_mfma_f32_32x32x16_bf16 v[34:49], v[84:87], v[92:95], v[34:49]
	v_cvt_pk_bf16_f32 v72, v70, v71
	v_cvt_pk_bf16_f32 v70, v66, v67
	v_add_f32_e32 v66, v104, v77
	v_cvt_pk_bf16_f32 v71, v68, v69
	v_rcp_f32_e32 v104, v66
	v_cvt_pk_bf16_f32 v69, v82, v83
	v_cvt_pk_bf16_f32 v68, v80, v81
	v_cvt_pk_bf16_f32 v67, v78, v79
	v_cvt_pk_bf16_f32 v66, v74, v75
	ds_read_b128 v[78:81], v150 offset:54272
	v_mfma_f32_32x32x16_bf16 v[50:65], v[88:91], v[70:73], v[50:65]
	v_mul_f32_e32 v2, v2, v76
	v_mul_f32_e32 v3, v3, v76
	v_mul_f32_e32 v20, v20, v104
	v_mul_f32_e32 v21, v21, v104
	v_cvt_pk_bf16_f32 v85, v8, v9
	v_cvt_pk_bf16_f32 v82, v2, v3
	v_pk_mul_f32 v[2:3], v[22:23], v[104:105] op_sel_hi:[1,0]
	v_pk_mul_f32 v[8:9], v[24:25], v[104:105] op_sel_hi:[1,0]
	v_pk_mul_f32 v[18:19], v[18:19], v[104:105] op_sel_hi:[1,0]
	v_mfma_f32_32x32x16_bf16 v[34:49], v[88:91], v[66:69], v[34:49]
	v_cvt_pk_bf16_f32 v84, v102, v103
	v_cvt_pk_bf16_f32 v83, v100, v101
	ds_read_b128 v[86:89], v150 offset:55296
	v_cvt_pk_bf16_f32 v99, v8, v9
	v_cvt_pk_bf16_f32 v98, v2, v3
	v_cvt_pk_bf16_f32 v97, v20, v21
	v_cvt_pk_bf16_f32 v96, v18, v19
	s_waitcnt lgkmcnt(1)
	v_mfma_f32_32x32x16_bf16 v[50:65], v[78:81], v[82:85], v[50:65]
	v_mul_f32_e32 v2, v14, v76
	v_mul_f32_e32 v3, v15, v76
	v_mul_f32_e32 v8, v16, v76
	v_mul_f32_e32 v9, v17, v76
	v_mul_f32_e32 v14, v26, v104
	v_mul_f32_e32 v15, v27, v104
	v_cvt_pk_bf16_f32 v77, v8, v9
	v_cvt_pk_bf16_f32 v76, v2, v3
	v_cvt_pk_bf16_f32 v74, v10, v11
	v_pk_mul_f32 v[2:3], v[28:29], v[104:105] op_sel_hi:[1,0]
	v_mfma_f32_32x32x16_bf16 v[34:49], v[78:81], v[96:99], v[34:49]
	v_mul_f32_e32 v8, v30, v104
	v_mul_f32_e32 v9, v31, v104
	v_mul_f32_e32 v10, v32, v104
	v_mul_f32_e32 v11, v33, v104
	v_cvt_pk_bf16_f32 v75, v12, v13
	v_cvt_pk_bf16_f32 v81, v10, v11
	v_cvt_pk_bf16_f32 v80, v8, v9
	v_cvt_pk_bf16_f32 v79, v2, v3
	v_cvt_pk_bf16_f32 v78, v14, v15
	s_waitcnt lgkmcnt(0)
	v_mfma_f32_32x32x16_bf16 v[50:65], v[86:89], v[74:77], v[50:65]
	v_mfma_f32_32x32x16_bf16 v[34:49], v[86:89], v[78:81], v[34:49]
	ds_read_b128 v[86:89], v150 offset:56320
	ds_read_b128 v[18:21], v150 offset:44032
	ds_read_b128 v[22:25], v150 offset:45056
	ds_read_b128 v[26:29], v150 offset:46080
	ds_read_b128 v[30:33], v150 offset:47104
	ds_read_b128 v[100:103], v150 offset:57344
	s_waitcnt lgkmcnt(1)
	v_mfma_f32_32x32x16_bf16 v[18:33], v[86:89], v[4:7], v[18:33]
	ds_read_b128 v[2:5], v150 offset:48128
	ds_read_b128 v[6:9], v150 offset:49152
	ds_read_b128 v[10:13], v150 offset:50176
	ds_read_b128 v[14:17], v150 offset:51200
	s_waitcnt lgkmcnt(0)
	v_mfma_f32_32x32x16_bf16 v[2:17], v[86:89], v[92:95], v[2:17]
	v_mfma_f32_32x32x16_bf16 v[18:33], v[100:103], v[70:73], v[18:33]
	v_mfma_f32_32x32x16_bf16 v[2:17], v[100:103], v[66:69], v[2:17]
	ds_read_b128 v[66:69], v150 offset:58368
	ds_read_b128 v[70:73], v150 offset:59392
	s_waitcnt lgkmcnt(1)
	v_mfma_f32_32x32x16_bf16 v[18:33], v[66:69], v[82:85], v[18:33]
	v_mfma_f32_32x32x16_bf16 v[2:17], v[66:69], v[96:99], v[2:17]
	s_waitcnt lgkmcnt(0)
	v_mfma_f32_32x32x16_bf16 v[18:33], v[70:73], v[74:77], v[18:33]
	v_mfma_f32_32x32x16_bf16 v[2:17], v[70:73], v[78:81], v[2:17]
	s_nop 10
	v_mul_f32_e32 v66, v22, v22
	v_mul_f32_e32 v67, v23, v23
	v_mul_f32_e32 v68, v30, v30
	v_mul_f32_e32 v69, v31, v31
	v_mul_f32_e32 v70, v24, v24
	v_mul_f32_e32 v71, v25, v25
	v_pk_mul_f32 v[72:73], v[32:33], v[32:33]
	v_pk_mul_f32 v[74:75], v[20:21], v[20:21]
	v_pk_mul_f32 v[76:77], v[28:29], v[28:29]
	v_pk_mul_f32 v[78:79], v[26:27], v[26:27]
	v_pk_mul_f32 v[80:81], v[18:19], v[18:19]
	v_pk_fma_f32 v[78:79], v[58:59], v[58:59], v[78:79]
	v_pk_fma_f32 v[76:77], v[60:61], v[60:61], v[76:77]
	v_pk_fma_f32 v[74:75], v[52:53], v[52:53], v[74:75]
	v_pk_fma_f32 v[72:73], v[64:65], v[64:65], v[72:73]
	v_pk_fma_f32 v[70:71], v[56:57], v[56:57], v[70:71]
	v_pk_fma_f32 v[68:69], v[62:63], v[62:63], v[68:69]
	v_pk_fma_f32 v[66:67], v[54:55], v[54:55], v[66:67]
	v_pk_fma_f32 v[80:81], v[50:51], v[50:51], v[80:81]
	v_pk_add_f32 v[66:67], v[66:67], v[68:69]
	v_pk_add_f32 v[68:69], v[70:71], v[72:73]
	v_pk_add_f32 v[70:71], v[74:75], v[76:77]
	v_pk_add_f32 v[72:73], v[80:81], v[78:79]
	v_pk_add_f32 v[68:69], v[70:71], v[68:69]
	v_pk_add_f32 v[66:67], v[72:73], v[66:67]
	v_pk_mul_f32 v[72:73], v[14:15], v[14:15]
	v_pk_mov_b32 v[70:71], v[66:67], v[68:69] op_sel:[1,0]
	v_mov_b32_e32 v67, v69
	v_pk_add_f32 v[66:67], v[70:71], v[66:67]
	v_pk_mul_f32 v[70:71], v[6:7], v[6:7]
	v_pk_mul_f32 v[74:75], v[8:9], v[8:9]
	v_pk_mul_f32 v[76:77], v[16:17], v[16:17]
	v_pk_mul_f32 v[78:79], v[4:5], v[4:5]
	v_pk_mul_f32 v[80:81], v[12:13], v[12:13]
	v_pk_mul_f32 v[82:83], v[10:11], v[10:11]
	v_pk_mul_f32 v[84:85], v[2:3], v[2:3]
	v_pk_fma_f32 v[82:83], v[42:43], v[42:43], v[82:83]
	v_pk_fma_f32 v[80:81], v[44:45], v[44:45], v[80:81]
	v_pk_fma_f32 v[78:79], v[36:37], v[36:37], v[78:79]
	v_pk_fma_f32 v[76:77], v[48:49], v[48:49], v[76:77]
	v_pk_fma_f32 v[74:75], v[40:41], v[40:41], v[74:75]
	v_pk_fma_f32 v[72:73], v[46:47], v[46:47], v[72:73]
	v_pk_fma_f32 v[70:71], v[38:39], v[38:39], v[70:71]
	v_pk_fma_f32 v[84:85], v[34:35], v[34:35], v[84:85]
	v_pk_add_f32 v[70:71], v[70:71], v[72:73]
	v_pk_add_f32 v[72:73], v[74:75], v[76:77]
	v_pk_add_f32 v[74:75], v[78:79], v[80:81]
	v_pk_add_f32 v[76:77], v[84:85], v[82:83]
	v_pk_add_f32 v[72:73], v[74:75], v[72:73]
	v_pk_add_f32 v[70:71], v[76:77], v[70:71]
	v_pk_add_f32 v[66:67], v[66:67], v[66:67] op_sel:[0,1] op_sel_hi:[1,0]
	v_pk_mov_b32 v[74:75], v[70:71], v[72:73] op_sel:[1,0]
	v_mov_b32_e32 v71, v73
	v_pk_add_f32 v[70:71], v[74:75], v[70:71]
	v_mov_b32_e32 v69, v66
	v_pk_add_f32 v[70:71], v[70:71], v[70:71] op_sel:[0,1] op_sel_hi:[1,0]
	s_nop 0
	v_permlane32_swap_b32_e32 v66, v69
	v_mov_b32_e32 v68, v70
	s_nop 1
	v_permlane32_swap_b32_e32 v70, v68
	v_mov_b32_e32 v71, v66
	v_pk_add_f32 v[66:67], v[70:71], v[68:69]
	v_pk_fma_f32 v[66:67], v[66:67], s[0:1], v[152:153] op_sel_hi:[1,0,0]
	s_mov_b32 s1, 0x800000
	v_mul_f32_e32 v68, 0x4b800000, v67
	v_cmp_gt_f32_e32 vcc, s1, v67
	s_nop 1
	v_cndmask_b32_e32 v67, v67, v68, vcc
	v_rsq_f32_e32 v67, v67
	s_nop 0
	v_mul_f32_e32 v68, 0x45800000, v67
	v_cndmask_b32_e32 v68, v67, v68, vcc
	v_pk_mul_f32 v[158:159], v[50:51], v[68:69] op_sel_hi:[1,0]
	v_pk_mul_f32 v[50:51], v[18:19], v[68:69] op_sel_hi:[1,0]
	v_mul_f32_e32 v18, 0x4b800000, v66
	v_cmp_gt_f32_e32 vcc, s1, v66
	v_pk_mul_f32 v[80:81], v[60:61], v[68:69] op_sel_hi:[1,0]
	v_pk_mul_f32 v[60:61], v[28:29], v[68:69] op_sel_hi:[1,0]
	v_cndmask_b32_e32 v18, v66, v18, vcc
	v_rsq_f32_e32 v18, v18
	v_pk_mul_f32 v[78:79], v[58:59], v[68:69] op_sel_hi:[1,0]
	v_pk_mul_f32 v[160:161], v[52:53], v[68:69] op_sel_hi:[1,0]
	v_pk_mul_f32 v[82:83], v[54:55], v[68:69] op_sel_hi:[1,0]
	v_mul_f32_e32 v19, 0x45800000, v18
	v_cndmask_b32_e32 v28, v18, v19, vcc
	v_pk_mul_f32 v[168:169], v[56:57], v[68:69] op_sel_hi:[1,0]
	v_pk_mul_f32 v[58:59], v[26:27], v[68:69] op_sel_hi:[1,0]
	v_pk_mul_f32 v[52:53], v[20:21], v[68:69] op_sel_hi:[1,0]
	v_pk_mul_f32 v[54:55], v[22:23], v[68:69] op_sel_hi:[1,0]
	v_pk_mul_f32 v[56:57], v[24:25], v[68:69] op_sel_hi:[1,0]
	v_pk_mul_f32 v[18:19], v[42:43], v[28:29] op_sel_hi:[1,0]
	v_pk_mul_f32 v[20:21], v[44:45], v[28:29] op_sel_hi:[1,0]
	v_pk_mul_f32 v[22:23], v[46:47], v[28:29] op_sel_hi:[1,0]
	v_pk_mul_f32 v[26:27], v[48:49], v[28:29] op_sel_hi:[1,0]
	v_pk_mul_f32 v[162:163], v[34:35], v[28:29] op_sel_hi:[1,0]
	v_pk_mul_f32 v[164:165], v[36:37], v[28:29] op_sel_hi:[1,0]
	v_pk_mul_f32 v[166:167], v[38:39], v[28:29] op_sel_hi:[1,0]
	v_pk_mul_f32 v[24:25], v[40:41], v[28:29] op_sel_hi:[1,0]
	v_pk_mul_f32 v[104:105], v[2:3], v[28:29] op_sel_hi:[1,0]
	v_pk_mul_f32 v[112:113], v[4:5], v[28:29] op_sel_hi:[1,0]
	ds_read_b128 v[2:5], v150 offset:60416
	ds_read_b128 v[34:37], v174 offset:32768
	ds_read_b128 v[38:41], v174 offset:32800
	ds_read_b128 v[42:45], v174 offset:32832
	ds_read_b128 v[46:49], v174 offset:32864
	v_cvt_pk_bf16_f32 v129, v168, v169
	v_cvt_pk_bf16_f32 v128, v82, v83
	v_cvt_pk_bf16_f32 v127, v160, v161
	v_cvt_pk_bf16_f32 v126, v158, v159
	v_cvt_pk_bf16_f32 v137, v24, v25
	v_cvt_pk_bf16_f32 v136, v166, v167
	v_cvt_pk_bf16_f32 v135, v164, v165
	s_waitcnt lgkmcnt(0)
	v_mfma_f32_32x32x16_bf16 v[86:101], v[2:5], v[126:129], v[34:49]
	v_cvt_pk_bf16_f32 v134, v162, v163
	v_mul_f32_e32 v84, v62, v68
	v_mul_f32_e32 v85, v63, v68
	v_mul_f32_e32 v170, v64, v68
	v_mul_f32_e32 v171, v65, v68
	v_pk_mul_f32 v[62:63], v[30:31], v[68:69] op_sel_hi:[1,0]
	v_pk_mul_f32 v[64:65], v[32:33], v[68:69] op_sel_hi:[1,0]
	v_pk_mul_f32 v[116:117], v[6:7], v[28:29] op_sel_hi:[1,0]
	v_pk_mul_f32 v[154:155], v[8:9], v[28:29] op_sel_hi:[1,0]
	v_mfma_f32_32x32x16_bf16 v[34:49], v[2:5], v[134:137], v[34:49]
	ds_read_b128 v[6:9], v150 offset:61440
	ds_read_b128 v[66:69], v174 offset:32896
	ds_read_b128 v[106:109], v150 offset:64512
	v_cvt_pk_bf16_f32 v125, v170, v171
	v_cvt_pk_bf16_f32 v124, v84, v85
	v_cvt_pk_bf16_f32 v123, v80, v81
	v_cvt_pk_bf16_f32 v122, v78, v79
	v_cvt_pk_bf16_f32 v149, v26, v27
	v_cvt_pk_bf16_f32 v148, v22, v23
	v_cvt_pk_bf16_f32 v147, v20, v21
	v_cvt_pk_bf16_f32 v146, v18, v19
	s_waitcnt lgkmcnt(2)
	v_mfma_f32_32x32x16_bf16 v[86:101], v[6:9], v[122:125], v[86:101]
	v_mul_f32_e32 v102, v10, v28
	v_mul_f32_e32 v103, v11, v28
	v_mul_f32_e32 v110, v12, v28
	v_mul_f32_e32 v111, v13, v28
	v_mul_f32_e32 v114, v14, v28
	v_mul_f32_e32 v115, v15, v28
	v_pk_mul_f32 v[156:157], v[16:17], v[28:29] op_sel_hi:[1,0]
	ds_read_b128 v[176:179], v174 offset:33536
	ds_read_b128 v[180:183], v174 offset:33568
	ds_read_b128 v[184:187], v174 offset:33600
	ds_read_b128 v[28:31], v174 offset:33632
	ds_read_b128 v[188:191], v174 offset:33792
	ds_read_b128 v[192:195], v174 offset:33824
	ds_read_b128 v[196:199], v174 offset:33856
	ds_read_b128 v[200:203], v174 offset:33888
	ds_read_b128 v[204:207], v150 offset:62464
	v_cvt_pk_bf16_f32 v133, v56, v57
	v_mfma_f32_32x32x16_bf16 v[34:49], v[6:9], v[146:149], v[34:49]
	v_cvt_pk_bf16_f32 v132, v54, v55
	v_cvt_pk_bf16_f32 v131, v52, v53
	v_cvt_pk_bf16_f32 v130, v50, v51
	ds_read_b128 v[70:73], v174 offset:33664
	ds_read_b128 v[74:77], v174 offset:33920
	ds_read_b128 v[208:211], v150 offset:63488
	v_cvt_pk_bf16_f32 v145, v154, v155
	v_cvt_pk_bf16_f32 v144, v116, v117
	v_cvt_pk_bf16_f32 v143, v112, v113
	v_cvt_pk_bf16_f32 v142, v104, v105
	s_waitcnt lgkmcnt(3)
	v_mfma_f32_32x32x16_bf16 v[86:101], v[204:207], v[130:133], v[86:101]
	v_cvt_pk_bf16_f32 v121, v64, v65
	v_cvt_pk_bf16_f32 v120, v62, v63
	v_cvt_pk_bf16_f32 v119, v60, v61
	v_cvt_pk_bf16_f32 v118, v58, v59
	v_cvt_pk_bf16_f32 v141, v156, v157
	v_cvt_pk_bf16_f32 v140, v114, v115
	v_cvt_pk_bf16_f32 v139, v110, v111
	v_mfma_f32_32x32x16_bf16 v[34:49], v[204:207], v[142:145], v[34:49]
	v_cvt_pk_bf16_f32 v138, v102, v103
	v_fma_f32 v16, v30, v170, v202
	v_fma_f32 v17, v31, v171, v203
	v_fma_f32 v14, v28, v84, v200
	v_fma_f32 v15, v29, v85, v201
	v_pk_fma_f32 v[12:13], v[186:187], v[80:81], v[198:199]
	v_pk_fma_f32 v[10:11], v[184:185], v[78:79], v[196:197]
	v_pk_fma_f32 v[8:9], v[182:183], v[168:169], v[194:195]
	s_waitcnt lgkmcnt(0)
	v_mfma_f32_32x32x16_bf16 v[86:101], v[208:211], v[118:121], v[86:101]
	v_fma_f32 v6, v180, v82, v192
	v_fma_f32 v7, v181, v83, v193
	ds_read_b128 v[78:81], v174 offset:33760
	ds_read_b128 v[82:85], v174 offset:33248
	v_fma_f32 v4, v178, v160, v190
	v_fma_f32 v5, v179, v161, v191
	v_pk_fma_f32 v[2:3], v[176:177], v[158:159], v[188:189]
	v_pk_fma_f32 v[32:33], v[30:31], v[26:27], v[202:203]
	v_pk_fma_f32 v[30:31], v[28:29], v[22:23], v[200:201]
	v_pk_fma_f32 v[28:29], v[186:187], v[20:21], v[198:199]
	v_pk_fma_f32 v[26:27], v[184:185], v[18:19], v[196:197]
	v_pk_fma_f32 v[24:25], v[182:183], v[24:25], v[194:195]
	v_pk_fma_f32 v[22:23], v[180:181], v[166:167], v[192:193]
	v_pk_fma_f32 v[20:21], v[178:179], v[164:165], v[190:191]
	v_pk_fma_f32 v[18:19], v[176:177], v[162:163], v[188:189]
	ds_read_b128 v[158:161], v174 offset:33696
	ds_read_b128 v[162:165], v174 offset:33728
	ds_read_b128 v[166:169], v174 offset:33952
	ds_read_b128 v[176:179], v174 offset:33984
	ds_read_b128 v[180:183], v174 offset:34016
	ds_read_b128 v[184:187], v212 offset:11264
	v_mfma_f32_32x32x16_bf16 v[34:49], v[208:211], v[138:141], v[34:49]
	v_cvt_pk_bf16_f32 v86, v86, v87
	v_cvt_pk_bf16_f32 v87, v88, v89
	v_cvt_pk_bf16_f32 v88, v90, v91
	v_cvt_pk_bf16_f32 v89, v92, v93
	ds_read_b128 v[90:93], v212 offset:12288
	v_pk_max_i16 v86, v86, 0
	v_pk_max_i16 v87, v87, 0
	v_pk_max_i16 v88, v88, 0
	v_pk_max_i16 v89, v89, 0
	s_nop 1
	s_nop 0
	v_cvt_pk_bf16_f32 v188, v34, v35
	v_cvt_pk_bf16_f32 v189, v36, v37
	v_cvt_pk_bf16_f32 v190, v38, v39
	v_cvt_pk_bf16_f32 v191, v40, v41
	s_waitcnt lgkmcnt(1)
	v_mfma_f32_32x32x16_bf16 v[2:17], v[184:187], v[86:89], v[2:17]
	v_pk_max_i16 v188, v188, 0
	v_pk_max_i16 v189, v189, 0
	v_pk_max_i16 v190, v190, 0
	v_pk_max_i16 v191, v191, 0
	v_cvt_pk_bf16_f32 v94, v94, v95
	v_cvt_pk_bf16_f32 v95, v96, v97
	v_cvt_pk_bf16_f32 v96, v98, v99
	v_cvt_pk_bf16_f32 v97, v100, v101
	v_cvt_pk_bf16_f32 v98, v42, v43
	v_cvt_pk_bf16_f32 v99, v44, v45
	v_mfma_f32_32x32x16_bf16 v[18:33], v[184:187], v[188:191], v[18:33]
	ds_read_b128 v[184:187], v212 offset:19456
	v_cvt_pk_bf16_f32 v100, v46, v47
	v_cvt_pk_bf16_f32 v101, v48, v49
	v_fma_f32 v64, v80, v64, v182
	v_fma_f32 v65, v81, v65, v183
	v_pk_fma_f32 v[62:63], v[78:79], v[62:63], v[180:181]
	v_pk_fma_f32 v[60:61], v[164:165], v[60:61], v[178:179]
	v_pk_fma_f32 v[58:59], v[162:163], v[58:59], v[176:177]
	v_pk_max_i16 v94, v94, 0
	v_pk_max_i16 v95, v95, 0
	v_pk_max_i16 v96, v96, 0
	v_pk_max_i16 v97, v97, 0
	v_pk_max_i16 v98, v98, 0
	v_pk_max_i16 v99, v99, 0
	v_pk_max_i16 v100, v100, 0
	v_pk_max_i16 v101, v101, 0
	v_pk_fma_f32 v[56:57], v[160:161], v[56:57], v[168:169]
	s_waitcnt lgkmcnt(1)
	v_mfma_f32_32x32x16_bf16 v[2:17], v[90:93], v[94:97], v[2:17]
	v_fma_f32 v54, v158, v54, v166
	v_fma_f32 v55, v159, v55, v167
	v_fma_f32 v52, v72, v52, v76
	v_fma_f32 v53, v73, v53, v77
	v_fma_f32 v50, v70, v50, v74
	v_fma_f32 v51, v71, v51, v75
	v_pk_fma_f32 v[48:49], v[80:81], v[156:157], v[182:183]
	v_pk_fma_f32 v[46:47], v[78:79], v[114:115], v[180:181]
	v_pk_fma_f32 v[44:45], v[164:165], v[110:111], v[178:179]
	v_pk_fma_f32 v[42:43], v[162:163], v[102:103], v[176:177]
	v_mfma_f32_32x32x16_bf16 v[18:33], v[90:93], v[98:101], v[18:33]
	ds_read_b128 v[90:93], v212 offset:20480
	v_fma_f32 v40, v160, v154, v168
	v_fma_f32 v41, v161, v155, v169
	v_fma_f32 v38, v158, v116, v166
	v_fma_f32 v39, v159, v117, v167
	v_pk_fma_f32 v[36:37], v[72:73], v[112:113], v[76:77]
	v_pk_fma_f32 v[34:35], v[70:71], v[104:105], v[74:75]
	s_waitcnt lgkmcnt(1)
	v_mfma_f32_32x32x16_bf16 v[50:65], v[184:187], v[86:89], v[50:65]
	ds_read_b128 v[70:73], v174 offset:32928
	ds_read_b128 v[74:77], v174 offset:32960
	ds_read_b128 v[78:81], v174 offset:32992
	ds_read_b128 v[86:89], v174 offset:33024
	ds_read_b128 v[110:113], v212 offset:1024
	v_mfma_f32_32x32x16_bf16 v[34:49], v[184:187], v[188:191], v[34:49]
	s_waitcnt lgkmcnt(5)
	v_mfma_f32_32x32x16_bf16 v[50:65], v[90:93], v[94:97], v[50:65]
	v_mfma_f32_32x32x16_bf16 v[34:49], v[90:93], v[98:101], v[34:49]
	s_waitcnt lgkmcnt(2)
	v_mfma_f32_32x32x16_bf16 v[90:105], v[106:109], v[126:129], v[66:81]
	v_mfma_f32_32x32x16_bf16 v[66:81], v[106:109], v[134:137], v[66:81]
	ds_read_b128 v[106:109], v212 offset:0
	s_waitcnt lgkmcnt(0)
	v_mfma_f32_32x32x16_bf16 v[90:105], v[106:109], v[122:125], v[90:105]
	v_mfma_f32_32x32x16_bf16 v[66:81], v[106:109], v[146:149], v[66:81]
	ds_read_b128 v[106:109], v212 offset:2048
	v_mfma_f32_32x32x16_bf16 v[90:105], v[110:113], v[130:133], v[90:105]
	v_mfma_f32_32x32x16_bf16 v[66:81], v[110:113], v[142:145], v[66:81]
	ds_read_b128 v[110:113], v212 offset:13312
	s_waitcnt lgkmcnt(1)
	v_mfma_f32_32x32x16_bf16 v[90:105], v[106:109], v[118:121], v[90:105]
	v_mfma_f32_32x32x16_bf16 v[66:81], v[106:109], v[138:141], v[66:81]
	s_nop 10
	v_cvt_pk_bf16_f32 v90, v90, v91
	v_cvt_pk_bf16_f32 v91, v92, v93
	v_cvt_pk_bf16_f32 v92, v94, v95
	v_cvt_pk_bf16_f32 v94, v98, v99
	v_cvt_pk_bf16_f32 v95, v100, v101
	ds_read_b128 v[98:101], v212 offset:21504
	v_cvt_pk_bf16_f32 v66, v66, v67
	v_cvt_pk_bf16_f32 v67, v68, v69
	v_cvt_pk_bf16_f32 v68, v70, v71
	v_cvt_pk_bf16_f32 v93, v96, v97
	v_cvt_pk_bf16_f32 v69, v72, v73
	ds_read_b128 v[70:73], v212 offset:14336
	v_pk_max_i16 v90, v90, 0
	v_pk_max_i16 v91, v91, 0
	v_pk_max_i16 v92, v92, 0
	v_pk_max_i16 v93, v93, 0
	v_pk_max_i16 v66, v66, 0
	v_pk_max_i16 v67, v67, 0
	v_pk_max_i16 v68, v68, 0
	v_pk_max_i16 v69, v69, 0
	v_cvt_pk_bf16_f32 v96, v102, v103
	s_waitcnt lgkmcnt(2)
	v_mfma_f32_32x32x16_bf16 v[2:17], v[110:113], v[90:93], v[2:17]
	v_cvt_pk_bf16_f32 v97, v104, v105
	v_cvt_pk_bf16_f32 v74, v74, v75
	v_cvt_pk_bf16_f32 v75, v76, v77
	v_cvt_pk_bf16_f32 v76, v78, v79
	v_cvt_pk_bf16_f32 v77, v80, v81
	v_pk_max_i16 v94, v94, 0
	v_pk_max_i16 v95, v95, 0
	v_pk_max_i16 v96, v96, 0
	v_pk_max_i16 v97, v97, 0
	v_pk_max_i16 v74, v74, 0
	v_pk_max_i16 v75, v75, 0
	v_pk_max_i16 v76, v76, 0
	v_pk_max_i16 v77, v77, 0
	v_mfma_f32_32x32x16_bf16 v[18:33], v[110:113], v[66:69], v[18:33]
	s_waitcnt lgkmcnt(1)
	v_mfma_f32_32x32x16_bf16 v[34:49], v[98:101], v[66:69], v[34:49]
	ds_read_b128 v[66:69], v212 offset:22528
	v_mfma_f32_32x32x16_bf16 v[50:65], v[98:101], v[90:93], v[50:65]
	s_waitcnt lgkmcnt(1)
	v_mfma_f32_32x32x16_bf16 v[2:17], v[70:73], v[94:97], v[2:17]
	v_mfma_f32_32x32x16_bf16 v[18:33], v[70:73], v[74:77], v[18:33]
	ds_read_b128 v[78:81], v212 offset:3072
	s_waitcnt lgkmcnt(1)
	v_mfma_f32_32x32x16_bf16 v[50:65], v[66:69], v[94:97], v[50:65]
	ds_read_b128 v[90:93], v174 offset:33056
	ds_read_b128 v[94:97], v174 offset:33088
	ds_read_b128 v[98:101], v174 offset:33120
	ds_read_b128 v[70:73], v174 offset:33152
	v_mfma_f32_32x32x16_bf16 v[34:49], v[66:69], v[74:77], v[34:49]
	ds_read_b128 v[66:69], v212 offset:4096
	ds_read_b128 v[74:77], v212 offset:5120
	s_waitcnt lgkmcnt(3)
	v_mfma_f32_32x32x16_bf16 v[102:117], v[78:81], v[126:129], v[86:101]
	v_mfma_f32_32x32x16_bf16 v[86:101], v[78:81], v[134:137], v[86:101]
	s_waitcnt lgkmcnt(1)
	v_mfma_f32_32x32x16_bf16 v[86:101], v[66:69], v[146:149], v[86:101]
	v_mfma_f32_32x32x16_bf16 v[102:117], v[66:69], v[122:125], v[102:117]
	ds_read_b128 v[66:69], v212 offset:6144
	s_waitcnt lgkmcnt(1)
	v_mfma_f32_32x32x16_bf16 v[86:101], v[74:77], v[142:145], v[86:101]
	v_mfma_f32_32x32x16_bf16 v[102:117], v[74:77], v[130:133], v[102:117]
	ds_read_b128 v[74:77], v212 offset:15360
	s_waitcnt lgkmcnt(1)
	v_mfma_f32_32x32x16_bf16 v[86:101], v[66:69], v[138:141], v[86:101]
	v_mfma_f32_32x32x16_bf16 v[102:117], v[66:69], v[118:121], v[102:117]
	s_nop 10
	v_cvt_pk_bf16_f32 v78, v86, v87
	v_cvt_pk_bf16_f32 v80, v90, v91
	v_cvt_pk_bf16_f32 v79, v88, v89
	v_cvt_pk_bf16_f32 v81, v92, v93
	ds_read_b128 v[86:89], v212 offset:16384
	ds_read_b128 v[90:93], v212 offset:23552
	v_cvt_pk_bf16_f32 v66, v102, v103
	v_cvt_pk_bf16_f32 v67, v104, v105
	v_cvt_pk_bf16_f32 v68, v106, v107
	v_cvt_pk_bf16_f32 v69, v108, v109
	v_pk_max_i16 v66, v66, 0
	v_pk_max_i16 v67, v67, 0
	v_pk_max_i16 v68, v68, 0
	v_pk_max_i16 v69, v69, 0
	v_pk_max_i16 v78, v78, 0
	v_pk_max_i16 v79, v79, 0
	v_pk_max_i16 v80, v80, 0
	v_pk_max_i16 v81, v81, 0
	v_cvt_pk_bf16_f32 v94, v94, v95
	s_waitcnt lgkmcnt(2)
	v_mfma_f32_32x32x16_bf16 v[18:33], v[74:77], v[78:81], v[18:33]
	v_cvt_pk_bf16_f32 v95, v96, v97
	v_cvt_pk_bf16_f32 v96, v98, v99
	v_cvt_pk_bf16_f32 v97, v100, v101
	v_pk_max_i16 v94, v94, 0
	v_pk_max_i16 v95, v95, 0
	v_pk_max_i16 v96, v96, 0
	v_pk_max_i16 v97, v97, 0
	v_mfma_f32_32x32x16_bf16 v[2:17], v[74:77], v[66:69], v[2:17]
	v_cvt_pk_bf16_f32 v74, v110, v111
	v_cvt_pk_bf16_f32 v75, v112, v113
	v_cvt_pk_bf16_f32 v76, v114, v115
	v_cvt_pk_bf16_f32 v77, v116, v117
	v_pk_max_i16 v74, v74, 0
	v_pk_max_i16 v75, v75, 0
	v_pk_max_i16 v76, v76, 0
	v_pk_max_i16 v77, v77, 0
	s_waitcnt lgkmcnt(0)
	v_mfma_f32_32x32x16_bf16 v[50:65], v[90:93], v[66:69], v[50:65]
	ds_read_b128 v[66:69], v212 offset:24576
	v_mfma_f32_32x32x16_bf16 v[34:49], v[90:93], v[78:81], v[34:49]
	ds_read_b128 v[102:105], v212 offset:7168
	v_mfma_f32_32x32x16_bf16 v[2:17], v[86:89], v[74:77], v[2:17]
	s_waitcnt lgkmcnt(1)
	v_mfma_f32_32x32x16_bf16 v[50:65], v[66:69], v[74:77], v[50:65]
	ds_read_b128 v[74:77], v174 offset:33184
	ds_read_b128 v[78:81], v174 offset:33216
	v_mfma_f32_32x32x16_bf16 v[34:49], v[66:69], v[94:97], v[34:49]
	ds_read_b128 v[66:69], v212 offset:8192
	v_mfma_f32_32x32x16_bf16 v[18:33], v[86:89], v[94:97], v[18:33]
	s_waitcnt lgkmcnt(1)
	v_mfma_f32_32x32x16_bf16 v[86:101], v[102:105], v[126:129], v[70:85]
	v_mfma_f32_32x32x16_bf16 v[70:85], v[102:105], v[134:137], v[70:85]
	ds_read_b128 v[102:105], v212 offset:9216
	v_lshlrev_b32_e32 v135, 2, v1
	v_add_u32_e32 v134, v172, v174
	s_waitcnt lgkmcnt(1)
	v_mfma_f32_32x32x16_bf16 v[86:101], v[66:69], v[122:125], v[86:101]
	v_mfma_f32_32x32x16_bf16 v[70:85], v[66:69], v[146:149], v[70:85]
	ds_read_b128 v[66:69], v212 offset:10240
	s_waitcnt lgkmcnt(1)
	v_mfma_f32_32x32x16_bf16 v[86:101], v[102:105], v[130:133], v[86:101]
	v_mfma_f32_32x32x16_bf16 v[70:85], v[102:105], v[142:145], v[70:85]
	ds_read_b128 v[102:105], v212 offset:17408
	s_waitcnt lgkmcnt(1)
	v_mfma_f32_32x32x16_bf16 v[86:101], v[66:69], v[118:121], v[86:101]
	v_mfma_f32_32x32x16_bf16 v[70:85], v[66:69], v[138:141], v[70:85]
	s_nop 10
	v_cvt_pk_bf16_f32 v68, v90, v91
	v_cvt_pk_bf16_f32 v69, v92, v93
	ds_read_b128 v[90:93], v212 offset:25600
	v_cvt_pk_bf16_f32 v66, v86, v87
	v_cvt_pk_bf16_f32 v67, v88, v89
	v_pk_max_i16 v66, v66, 0
	v_pk_max_i16 v67, v67, 0
	v_pk_max_i16 v68, v68, 0
	v_pk_max_i16 v69, v69, 0
	v_cvt_pk_bf16_f32 v70, v70, v71
	v_cvt_pk_bf16_f32 v71, v72, v73
	s_waitcnt lgkmcnt(1)
	v_mfma_f32_32x32x16_bf16 v[2:17], v[102:105], v[66:69], v[2:17]
	v_cvt_pk_bf16_f32 v72, v74, v75
	v_cvt_pk_bf16_f32 v73, v76, v77
	ds_read_b128 v[74:77], v212 offset:18432
	v_cvt_pk_bf16_f32 v86, v94, v95
	v_cvt_pk_bf16_f32 v87, v96, v97
	v_cvt_pk_bf16_f32 v88, v98, v99
	s_waitcnt lgkmcnt(1)
	v_mfma_f32_32x32x16_bf16 v[50:65], v[90:93], v[66:69], v[50:65]
	ds_read_b128 v[66:69], v212 offset:26624
	v_cvt_pk_bf16_f32 v89, v100, v101
	v_pk_max_i16 v86, v86, 0
	v_pk_max_i16 v87, v87, 0
	v_pk_max_i16 v88, v88, 0
	v_pk_max_i16 v89, v89, 0
	v_pk_max_i16 v70, v70, 0
	v_pk_max_i16 v71, v71, 0
	v_pk_max_i16 v72, v72, 0
	v_pk_max_i16 v73, v73, 0
	v_cvt_pk_bf16_f32 v78, v78, v79
	v_cvt_pk_bf16_f32 v79, v80, v81
	s_waitcnt lgkmcnt(1)
	v_mfma_f32_32x32x16_bf16 v[2:17], v[74:77], v[86:89], v[2:17]
	v_cvt_pk_bf16_f32 v80, v82, v83
	v_cvt_pk_bf16_f32 v81, v84, v85
	v_pk_max_i16 v78, v78, 0
	v_pk_max_i16 v79, v79, 0
	v_pk_max_i16 v80, v80, 0
	v_pk_max_i16 v81, v81, 0
	s_waitcnt lgkmcnt(0)
	v_mfma_f32_32x32x16_bf16 v[50:65], v[66:69], v[86:89], v[50:65]
	v_mfma_f32_32x32x16_bf16 v[34:49], v[90:93], v[70:73], v[34:49]
	s_nop 10
	v_add_f32_e32 v130, v10, v58
	v_add_f32_e32 v131, v11, v59
	v_add_f32_e32 v132, v12, v60
	v_add_f32_e32 v133, v13, v61
	v_add_f32_e32 v138, v4, v52
	v_add_f32_e32 v139, v5, v53
	v_pk_add_f32 v[140:141], v[16:17], v[64:65]
	v_pk_add_f32 v[142:143], v[8:9], v[56:57]
	v_pk_add_f32 v[144:145], v[14:15], v[62:63]
	v_pk_add_f32 v[146:147], v[6:7], v[54:55]
	v_mfma_f32_32x32x16_bf16 v[18:33], v[102:105], v[70:73], v[18:33]
	ds_read2st64_b32 v[70:71], v135 offset0:133 offset1:134
	v_add_f32_e32 v148, v2, v50
	v_add_f32_e32 v149, v3, v51
	v_add_f32_e32 v144, v146, v144
	v_add_f32_e32 v145, v147, v145
	v_pk_add_f32 v[140:141], v[142:143], v[140:141]
	v_pk_add_f32 v[132:133], v[138:139], v[132:133]
	v_pk_add_f32 v[130:131], v[148:149], v[130:131]
	v_pk_add_f32 v[132:133], v[132:133], v[140:141]
	v_pk_add_f32 v[130:131], v[130:131], v[144:145]
	v_mfma_f32_32x32x16_bf16 v[34:49], v[66:69], v[78:81], v[34:49]
	v_pk_mov_b32 v[138:139], v[130:131], v[132:133] op_sel:[1,0]
	v_mov_b32_e32 v131, v133
	s_waitcnt vmcnt(0) lgkmcnt(0)
	v_mul_f32_e32 v66, v175, v70
	v_pk_add_f32 v[130:131], v[138:139], v[130:131]
	ds_write_b32 v173, v66 offset:512
	v_mul_f32_e32 v66, v175, v71
	v_pk_add_f32 v[130:131], v[130:131], v[130:131] op_sel:[0,1] op_sel_hi:[1,0]
	s_waitcnt lgkmcnt(0)
	ds_read_b128 v[102:105], v174 offset:34560
	ds_read_b128 v[98:101], v174 offset:34592
	ds_read_b128 v[110:113], v174 offset:34624
	ds_read_b128 v[106:109], v174 offset:34656
	ds_read_b128 v[114:117], v174 offset:34688
	ds_read_b128 v[122:125], v174 offset:34720
	ds_read_b128 v[118:121], v174 offset:34752
	ds_read_b128 v[126:129], v174 offset:34784
	v_mov_b32_dpp v66, v66 quad_perm:[1,0,3,2] row_mask:0xf bank_mask:0xf bound_ctrl:1
	v_mov_b32_e32 v131, v130
	v_fmac_f32_e32 v66, v175, v71
	s_nop 0
	v_permlane32_swap_b32_e32 v130, v131
	v_add_f32_dpp v66, v66, v66 quad_perm:[2,3,0,1] row_mask:0xf bank_mask:0xf bound_ctrl:1
	v_add_f32_e32 v130, v130, v131
	v_fmamk_f32 v65, v130, 0xbc800000, v65
	v_add_f32_dpp v66, v66, v66 row_half_mirror row_mask:0xf bank_mask:0xf bound_ctrl:1
	v_fmamk_f32 v64, v130, 0xbc800000, v64
	v_fmamk_f32 v63, v130, 0xbc800000, v63
	v_fmamk_f32 v62, v130, 0xbc800000, v62
	v_fmamk_f32 v61, v130, 0xbc800000, v61
	v_fmamk_f32 v60, v130, 0xbc800000, v60
	v_fmamk_f32 v59, v130, 0xbc800000, v59
	v_fmamk_f32 v58, v130, 0xbc800000, v58
	v_fmamk_f32 v57, v130, 0xbc800000, v57
	v_fmamk_f32 v56, v130, 0xbc800000, v56
	v_fmamk_f32 v55, v130, 0xbc800000, v55
	v_fmamk_f32 v54, v130, 0xbc800000, v54
	v_fmamk_f32 v53, v130, 0xbc800000, v53
	v_fmamk_f32 v52, v130, 0xbc800000, v52
	v_fmamk_f32 v51, v130, 0xbc800000, v51
	v_fmac_f32_e32 v50, 0xbc800000, v130
	v_add_f32_dpp v66, v66, v66 row_ror:8 row_mask:0xf bank_mask:0xf bound_ctrl:1
	v_fmamk_f32 v17, v130, 0xbc800000, v17
	v_fmamk_f32 v16, v130, 0xbc800000, v16
	v_fmamk_f32 v15, v130, 0xbc800000, v15
	v_fmamk_f32 v14, v130, 0xbc800000, v14
	v_fmamk_f32 v13, v130, 0xbc800000, v13
	v_fmamk_f32 v12, v130, 0xbc800000, v12
	v_fmamk_f32 v11, v130, 0xbc800000, v11
	v_fmamk_f32 v10, v130, 0xbc800000, v10
	v_fmamk_f32 v9, v130, 0xbc800000, v9
	v_fmamk_f32 v8, v130, 0xbc800000, v8
	v_fmamk_f32 v7, v130, 0xbc800000, v7
	v_fmamk_f32 v6, v130, 0xbc800000, v6
	v_fmamk_f32 v5, v130, 0xbc800000, v5
	v_fmamk_f32 v4, v130, 0xbc800000, v4
	v_fmamk_f32 v3, v130, 0xbc800000, v3
	v_fmac_f32_e32 v2, 0xbc800000, v130
	v_pk_mul_f32 v[130:131], v[54:55], v[54:55]
	v_pk_mul_f32 v[132:133], v[62:63], v[62:63]
	v_pk_mul_f32 v[138:139], v[50:51], v[50:51]
	v_pk_mul_f32 v[140:141], v[58:59], v[58:59]
	v_pk_mul_f32 v[142:143], v[56:57], v[56:57]
	v_pk_mul_f32 v[144:145], v[64:65], v[64:65]
	v_pk_mul_f32 v[146:147], v[52:53], v[52:53]
	v_pk_mul_f32 v[148:149], v[60:61], v[60:61]
	v_mov_b32_e32 v67, v66
	v_pk_fma_f32 v[148:149], v[12:13], v[12:13], v[148:149]
	v_pk_fma_f32 v[146:147], v[4:5], v[4:5], v[146:147]
	v_pk_fma_f32 v[144:145], v[16:17], v[16:17], v[144:145]
	v_pk_fma_f32 v[142:143], v[8:9], v[8:9], v[142:143]
	v_pk_fma_f32 v[140:141], v[10:11], v[10:11], v[140:141]
	v_pk_fma_f32 v[138:139], v[2:3], v[2:3], v[138:139]
	v_pk_fma_f32 v[132:133], v[14:15], v[14:15], v[132:133]
	v_pk_fma_f32 v[130:131], v[6:7], v[6:7], v[130:131]
	v_permlane16_swap_b32_e32 v66, v67
	v_pk_add_f32 v[130:131], v[130:131], v[132:133]
	v_pk_add_f32 v[132:133], v[138:139], v[140:141]
	v_pk_add_f32 v[138:139], v[142:143], v[144:145]
	v_pk_add_f32 v[140:141], v[146:147], v[148:149]
	v_mfma_f32_32x32x16_bf16 v[18:33], v[74:77], v[78:81], v[18:33]
	v_add_f32_e32 v136, v66, v67
	ds_read_b128 v[70:73], v134 offset:512
	ds_read_b128 v[66:69], v134 offset:544
	ds_read_b128 v[78:81], v134 offset:576
	ds_read_b128 v[74:77], v134 offset:608
	ds_read_b128 v[82:85], v134 offset:640
	ds_read_b128 v[90:93], v134 offset:672
	ds_read_b128 v[86:89], v134 offset:704
	ds_read_b128 v[94:97], v134 offset:736
	v_pk_add_f32 v[138:139], v[140:141], v[138:139]
	v_pk_add_f32 v[130:131], v[132:133], v[130:131]
	s_waitcnt lgkmcnt(8)
	v_pk_mul_f32 v[140:141], v[126:127], v[62:63]
	v_pk_mov_b32 v[132:133], v[130:131], v[138:139] op_sel:[1,0]
	v_mov_b32_e32 v131, v139
	v_pk_mul_f32 v[138:139], v[122:123], v[54:55]
	v_pk_mul_f32 v[142:143], v[114:115], v[50:51]
	v_pk_mul_f32 v[144:145], v[118:119], v[58:59]
	v_pk_mul_f32 v[146:147], v[124:125], v[56:57]
	v_pk_mul_f32 v[148:149], v[128:129], v[64:65]
	v_pk_mul_f32 v[154:155], v[116:117], v[52:53]
	v_pk_mul_f32 v[156:157], v[120:121], v[60:61]
	v_pk_fma_f32 v[154:155], v[104:105], v[4:5], v[154:155]
	v_pk_fma_f32 v[156:157], v[112:113], v[12:13], v[156:157]
	v_pk_fma_f32 v[148:149], v[108:109], v[16:17], v[148:149]
	v_pk_fma_f32 v[146:147], v[100:101], v[8:9], v[146:147]
	v_pk_fma_f32 v[144:145], v[110:111], v[10:11], v[144:145]
	v_pk_fma_f32 v[142:143], v[102:103], v[2:3], v[142:143]
	v_pk_fma_f32 v[140:141], v[106:107], v[14:15], v[140:141]
	v_pk_fma_f32 v[138:139], v[98:99], v[6:7], v[138:139]
	v_pk_add_f32 v[130:131], v[132:133], v[130:131]
	v_pk_add_f32 v[138:139], v[138:139], v[140:141]
	v_pk_add_f32 v[140:141], v[142:143], v[144:145]
	v_pk_add_f32 v[142:143], v[146:147], v[148:149]
	v_pk_add_f32 v[144:145], v[154:155], v[156:157]
	v_pk_add_f32 v[132:133], v[130:131], v[130:131] op_sel:[0,1] op_sel_hi:[1,0]
	v_pk_add_f32 v[142:143], v[144:145], v[142:143]
	v_pk_add_f32 v[138:139], v[140:141], v[138:139]
	v_add_f32_e32 v133, v142, v143
	v_add_f32_e32 v130, v138, v139
	s_waitcnt lgkmcnt(2)
	v_pk_mul_f32 v[138:139], v[90:91], v[54:55]
	s_waitcnt lgkmcnt(0)
	v_pk_mul_f32 v[140:141], v[94:95], v[62:63]
	v_pk_mul_f32 v[142:143], v[82:83], v[50:51]
	v_pk_mul_f32 v[144:145], v[86:87], v[58:59]
	v_pk_mul_f32 v[146:147], v[92:93], v[56:57]
	v_pk_mul_f32 v[148:149], v[96:97], v[64:65]
	v_pk_mul_f32 v[154:155], v[84:85], v[52:53]
	v_pk_mul_f32 v[156:157], v[88:89], v[60:61]
	v_add_f32_e32 v130, v130, v133
	v_pk_fma_f32 v[156:157], v[80:81], v[12:13], v[156:157]
	v_pk_fma_f32 v[154:155], v[72:73], v[4:5], v[154:155]
	v_pk_fma_f32 v[148:149], v[76:77], v[16:17], v[148:149]
	v_pk_fma_f32 v[146:147], v[68:69], v[8:9], v[146:147]
	v_pk_fma_f32 v[144:145], v[78:79], v[10:11], v[144:145]
	v_pk_fma_f32 v[142:143], v[70:71], v[2:3], v[142:143]
	v_pk_fma_f32 v[140:141], v[74:75], v[14:15], v[140:141]
	v_pk_fma_f32 v[138:139], v[66:67], v[6:7], v[138:139]
	v_mov_b32_e32 v133, v130
	v_pk_add_f32 v[138:139], v[138:139], v[140:141]
	v_pk_add_f32 v[140:141], v[142:143], v[144:145]
	v_pk_add_f32 v[142:143], v[146:147], v[148:149]
	v_pk_add_f32 v[144:145], v[154:155], v[156:157]
	v_permlane32_swap_b32_e32 v130, v133
	v_pk_add_f32 v[142:143], v[144:145], v[142:143]
	v_add_f32_e32 v160, v130, v133
	v_pk_add_f32 v[138:139], v[140:141], v[138:139]
	v_add_f32_e32 v133, v142, v143
	v_pk_add_f32 v[140:141], v[26:27], v[42:43]
	v_pk_add_f32 v[142:143], v[28:29], v[44:45]
	v_pk_add_f32 v[144:145], v[20:21], v[36:37]
	v_pk_add_f32 v[146:147], v[32:33], v[48:49]
	v_pk_add_f32 v[148:149], v[24:25], v[40:41]
	v_pk_add_f32 v[154:155], v[30:31], v[46:47]
	v_pk_add_f32 v[156:157], v[22:23], v[38:39]
	v_pk_add_f32 v[158:159], v[18:19], v[34:35]
	v_pk_add_f32 v[154:155], v[156:157], v[154:155]
	v_pk_add_f32 v[146:147], v[148:149], v[146:147]
	v_pk_add_f32 v[142:143], v[144:145], v[142:143]
	v_pk_add_f32 v[140:141], v[158:159], v[140:141]
	v_pk_add_f32 v[142:143], v[142:143], v[146:147]
	v_pk_add_f32 v[140:141], v[140:141], v[154:155]
	v_add_f32_e32 v130, v138, v139
	v_pk_mov_b32 v[144:145], v[140:141], v[142:143] op_sel:[1,0]
	v_mov_b32_e32 v141, v143
	v_pk_add_f32 v[140:141], v[144:145], v[140:141]
	v_add_f32_e32 v133, v130, v133
	v_pk_add_f32 v[140:141], v[140:141], v[140:141] op_sel:[0,1] op_sel_hi:[1,0]
	v_mov_b32_e32 v131, v132
	v_mov_b32_e32 v130, v140
	s_nop 1
	v_permlane32_swap_b32_e32 v140, v130
	v_add_f32_e32 v130, v140, v130
	v_fmamk_f32 v49, v130, 0xbc800000, v49
	v_fmamk_f32 v48, v130, 0xbc800000, v48
	v_fmamk_f32 v47, v130, 0xbc800000, v47
	v_fmamk_f32 v46, v130, 0xbc800000, v46
	v_fmamk_f32 v45, v130, 0xbc800000, v45
	v_fmamk_f32 v44, v130, 0xbc800000, v44
	v_fmamk_f32 v43, v130, 0xbc800000, v43
	v_fmamk_f32 v42, v130, 0xbc800000, v42
	v_fmamk_f32 v41, v130, 0xbc800000, v41
	v_fmamk_f32 v40, v130, 0xbc800000, v40
	v_fmamk_f32 v39, v130, 0xbc800000, v39
	v_fmamk_f32 v38, v130, 0xbc800000, v38
	v_fmamk_f32 v37, v130, 0xbc800000, v37
	v_fmamk_f32 v36, v130, 0xbc800000, v36
	v_fmamk_f32 v35, v130, 0xbc800000, v35
	v_fmac_f32_e32 v34, 0xbc800000, v130
	v_fmamk_f32 v33, v130, 0xbc800000, v33
	v_fmamk_f32 v32, v130, 0xbc800000, v32
	v_fmamk_f32 v31, v130, 0xbc800000, v31
	v_fmamk_f32 v30, v130, 0xbc800000, v30
	v_fmamk_f32 v29, v130, 0xbc800000, v29
	v_fmamk_f32 v28, v130, 0xbc800000, v28
	v_fmamk_f32 v27, v130, 0xbc800000, v27
	v_fmamk_f32 v26, v130, 0xbc800000, v26
	v_fmamk_f32 v25, v130, 0xbc800000, v25
	v_fmamk_f32 v24, v130, 0xbc800000, v24
	v_fmamk_f32 v23, v130, 0xbc800000, v23
	v_fmamk_f32 v22, v130, 0xbc800000, v22
	v_fmamk_f32 v21, v130, 0xbc800000, v21
	v_fmamk_f32 v20, v130, 0xbc800000, v20
	v_fmamk_f32 v19, v130, 0xbc800000, v19
	v_fmac_f32_e32 v18, 0xbc800000, v130
	v_pk_mul_f32 v[140:141], v[38:39], v[38:39]
	v_pk_mul_f32 v[142:143], v[46:47], v[46:47]
	v_pk_mul_f32 v[144:145], v[34:35], v[34:35]
	v_pk_mul_f32 v[146:147], v[42:43], v[42:43]
	v_pk_mul_f32 v[148:149], v[40:41], v[40:41]
	v_pk_mul_f32 v[154:155], v[48:49], v[48:49]
	v_pk_mul_f32 v[156:157], v[36:37], v[36:37]
	v_pk_mul_f32 v[158:159], v[44:45], v[44:45]
	v_pk_fma_f32 v[156:157], v[20:21], v[20:21], v[156:157]
	v_pk_fma_f32 v[158:159], v[28:29], v[28:29], v[158:159]
	v_pk_fma_f32 v[154:155], v[32:33], v[32:33], v[154:155]
	v_pk_fma_f32 v[148:149], v[24:25], v[24:25], v[148:149]
	v_pk_fma_f32 v[146:147], v[26:27], v[26:27], v[146:147]
	v_pk_fma_f32 v[144:145], v[18:19], v[18:19], v[144:145]
	v_pk_fma_f32 v[142:143], v[30:31], v[30:31], v[142:143]
	v_pk_fma_f32 v[140:141], v[22:23], v[22:23], v[140:141]
	v_permlane32_swap_b32_e32 v132, v131
	v_pk_add_f32 v[140:141], v[140:141], v[142:143]
	v_pk_add_f32 v[142:143], v[144:145], v[146:147]
	v_pk_add_f32 v[144:145], v[148:149], v[154:155]
	v_pk_add_f32 v[146:147], v[156:157], v[158:159]
	v_pk_add_f32 v[140:141], v[142:143], v[140:141]
	v_pk_add_f32 v[144:145], v[146:147], v[144:145]
	v_pk_mul_f32 v[122:123], v[122:123], v[38:39]
	v_pk_mov_b32 v[142:143], v[140:141], v[144:145] op_sel:[1,0]
	v_mov_b32_e32 v141, v145
	v_pk_add_f32 v[140:141], v[142:143], v[140:141]
	v_pk_mul_f32 v[126:127], v[126:127], v[46:47]
	v_pk_add_f32 v[140:141], v[140:141], v[140:141] op_sel:[0,1] op_sel_hi:[1,0]
	v_pk_mul_f32 v[114:115], v[114:115], v[34:35]
	v_mov_b32_e32 v130, v140
	s_nop 1
	v_permlane32_swap_b32_e32 v140, v130
	v_mov_b32_e32 v141, v132
	v_pk_add_f32 v[130:131], v[140:141], v[130:131]
	v_pk_mul_f32 v[118:119], v[118:119], v[42:43]
	v_pk_fma_f32 v[130:131], v[130:131], s[0:1], v[152:153] op_sel_hi:[1,0,0]
	v_pk_mul_f32 v[124:125], v[124:125], v[40:41]
	v_mul_f32_e32 v132, 0x4b800000, v131
	v_cmp_gt_f32_e32 vcc, s1, v131
	v_pk_mul_f32 v[128:129], v[128:129], v[48:49]
	v_pk_mul_f32 v[116:117], v[116:117], v[36:37]
	v_pk_mul_f32 v[120:121], v[120:121], v[44:45]
	v_cndmask_b32_e32 v131, v131, v132, vcc
	v_mul_f32_e32 v132, 0x4b800000, v130
	v_cmp_gt_f32_e64 s[0:1], s1, v130
	v_pk_fma_f32 v[112:113], v[112:113], v[28:29], v[120:121]
	v_pk_fma_f32 v[104:105], v[104:105], v[20:21], v[116:117]
	v_pk_fma_f32 v[108:109], v[108:109], v[32:33], v[128:129]
	v_pk_fma_f32 v[100:101], v[100:101], v[24:25], v[124:125]
	v_pk_fma_f32 v[110:111], v[110:111], v[26:27], v[118:119]
	v_pk_fma_f32 v[102:103], v[102:103], v[18:19], v[114:115]
	v_pk_fma_f32 v[106:107], v[106:107], v[30:31], v[126:127]
	v_pk_fma_f32 v[98:99], v[98:99], v[22:23], v[122:123]
	v_rsq_f32_e32 v131, v131
	v_cndmask_b32_e64 v130, v130, v132, s[0:1]
	v_pk_add_f32 v[98:99], v[98:99], v[106:107]
	v_pk_add_f32 v[102:103], v[102:103], v[110:111]
	v_pk_add_f32 v[100:101], v[100:101], v[108:109]
	v_pk_add_f32 v[104:105], v[104:105], v[112:113]
	v_rsq_f32_e32 v132, v130
	v_pk_add_f32 v[100:101], v[104:105], v[100:101]
	v_pk_add_f32 v[98:99], v[102:103], v[98:99]
	v_mul_f32_e32 v130, 0x45800000, v131
	v_add_f32_e32 v98, v98, v99
	v_add_f32_e32 v99, v100, v101
	v_add_f32_e32 v98, v98, v99
	v_mov_b32_e32 v99, v98
	v_pk_mul_f32 v[90:91], v[90:91], v[38:39]
	v_pk_mul_f32 v[94:95], v[94:95], v[46:47]
	v_pk_mul_f32 v[82:83], v[82:83], v[34:35]
	v_pk_mul_f32 v[86:87], v[86:87], v[42:43]
	v_cndmask_b32_e32 v130, v131, v130, vcc
	v_mul_f32_e32 v131, 0x45800000, v132
	v_permlane32_swap_b32_e32 v98, v99
	v_pk_fma_f32 v[78:79], v[78:79], v[26:27], v[86:87]
	v_pk_fma_f32 v[70:71], v[70:71], v[18:19], v[82:83]
	v_pk_fma_f32 v[74:75], v[74:75], v[30:31], v[94:95]
	v_pk_fma_f32 v[66:67], v[66:67], v[22:23], v[90:91]
	v_cndmask_b32_e64 v131, v132, v131, s[0:1]
	v_add_f32_e32 v98, v98, v99
	v_pk_add_f32 v[66:67], v[66:67], v[74:75]
	v_pk_add_f32 v[70:71], v[70:71], v[78:79]
	v_mul_f32_e32 v139, v160, v130
	v_mul_f32_e32 v98, v98, v131
	v_pk_add_f32 v[66:67], v[70:71], v[66:67]
	v_cmp_gt_u32_e32 vcc, 32, v1
	v_add_f32_e32 v66, v66, v67
	v_pk_mul_f32 v[92:93], v[92:93], v[40:41]
	v_cndmask_b32_e32 v67, v98, v139, vcc
	v_add_f32_e32 v67, s12, v67
	v_pk_mul_f32 v[96:97], v[96:97], v[48:49]
	v_pk_mul_f32 v[84:85], v[84:85], v[36:37]
	v_pk_mul_f32 v[88:89], v[88:89], v[44:45]
	v_mul_f32_e32 v67, 0xbfb8aa3b, v67
	v_pk_fma_f32 v[80:81], v[80:81], v[28:29], v[88:89]
	v_pk_fma_f32 v[72:73], v[72:73], v[20:21], v[84:85]
	v_pk_fma_f32 v[76:77], v[76:77], v[32:33], v[96:97]
	v_pk_fma_f32 v[68:69], v[68:69], v[24:25], v[92:93]
	v_exp_f32_e32 v70, v67
	v_pk_add_f32 v[68:69], v[68:69], v[76:77]
	v_pk_add_f32 v[72:73], v[72:73], v[80:81]
	v_cmp_lt_i32_e64 s[0:1], 0, v151
	v_pk_add_f32 v[68:69], v[72:73], v[68:69]
	v_mov_b32_e32 v137, v136
	v_add_f32_e32 v67, v68, v69
	v_add_f32_e32 v67, v66, v67
	v_add_f32_e32 v66, 1.0, v70
	v_rcp_f32_e32 v66, v66
	v_mov_b32_e32 v69, 0xff800000
	v_mov_b32_e32 v138, v133
	v_mov_b32_e32 v68, v67
	v_cndmask_b32_e64 v70, v69, v66, s[0:1]
	v_mbcnt_lo_u32_b32 v66, -1, 0
	v_mbcnt_hi_u32_b32 v66, -1, v66
	v_permlane32_swap_b32_e32 v136, v137
	v_permlane32_swap_b32_e32 v133, v138
	v_permlane32_swap_b32_e32 v67, v68
	v_and_b32_e32 v86, 64, v66
	s_mov_b32 s14, 8
	s_mov_b32 s13, 0
	v_mov_b32_e32 v66, 0
	s_waitcnt lgkmcnt(0)
